# speedup vs baseline: 1.0174x; 1.0174x over previous
.LBB3_16:
	s_or_b64 exec, exec, s[4:5]
	v_and_b32_e32 v92, 63, v0
	s_lshr_b32 s27, s26, 6
	v_lshlrev_b32_e32 v30, 2, v0
	v_mov_b32_e32 v31, -1
	v_mov_b32_e32 v34, 0
	v_cmp_gt_u32_e64 s[14:15], 12, v0
	s_and_saveexec_b64 s[16:17], s[14:15]
	ds_write_b32 v30, v31 offset:54144
	s_mov_b64 exec, s[16:17]
	s_waitcnt vmcnt(0)
	v_add_u32_e32 v42, v2, v3
	v_add_u32_e32 v52, v11, v5
	v_add_u32_e32 v43, v8, v42
	v_add_u32_e32 v53, v4, v52
	v_add_u32_e32 v44, v9, v43
	v_add_u32_e32 v54, v1, v53
	v_add_u32_e32 v45, v10, v44
	v_add_u32_e32 v55, v16, v54
	v_add_u32_e32 v46, v12, v45
	v_add_u32_e32 v56, v15, v55
	v_add_u32_e32 v47, v13, v46
	v_add_u32_e32 v57, v21, v56
	v_add_u32_e32 v48, v14, v47
	v_add_u32_e32 v58, v17, v57
	v_add_u32_e32 v49, 0x7f, v48
	v_add_u32_e32 v59, 0x7f, v58
	v_lshrrev_b32_e32 v49, 7, v49
	v_lshrrev_b32_e32 v59, 7, v59
	v_mov_b32_e32 v50, v49
	v_mov_b32_e32 v51, v59
	s_nop 0
	v_add_u32_dpp v50, v50, v50 row_shr:1 row_mask:0xf bank_mask:0xf
	v_add_u32_dpp v51, v51, v51 row_shr:1 row_mask:0xf bank_mask:0xf
	s_nop 0
	v_add_u32_dpp v50, v50, v50 row_shr:2 row_mask:0xf bank_mask:0xf
	v_add_u32_dpp v51, v51, v51 row_shr:2 row_mask:0xf bank_mask:0xf
	s_nop 0
	v_add_u32_dpp v50, v50, v50 row_shr:4 row_mask:0xf bank_mask:0xf
	v_add_u32_dpp v51, v51, v51 row_shr:4 row_mask:0xf bank_mask:0xf
	s_nop 0
	v_add_u32_dpp v50, v50, v50 row_shr:8 row_mask:0xf bank_mask:0xf
	v_add_u32_dpp v51, v51, v51 row_shr:8 row_mask:0xf bank_mask:0xf
	s_nop 0
	v_add_u32_dpp v50, v50, v50 row_bcast:15 row_mask:0xa bank_mask:0xf
	v_add_u32_dpp v51, v51, v51 row_bcast:15 row_mask:0xa bank_mask:0xf
	s_nop 0
	v_add_u32_dpp v50, v50, v50 row_bcast:31 row_mask:0xc bank_mask:0xf
	v_add_u32_dpp v51, v51, v51 row_bcast:31 row_mask:0xc bank_mask:0xf
	s_nop 0
	v_readlane_b32 s6, v50, 63
	s_lshl_b32 s7, s27, 2
	v_mov_b32_e32 v33, s7
	v_cmp_eq_u32_e64 s[14:15], 0, v92
	v_mov_b32_e32 v32, s6
	s_and_saveexec_b64 s[16:17], s[14:15]
	ds_write_b32 v33, v32 offset:54192
	s_mov_b64 exec, s[16:17]
	s_waitcnt lgkmcnt(0)
	s_barrier
	ds_read_b128 v[64:67], v34 offset:54192
	s_waitcnt lgkmcnt(0)
	v_readfirstlane_b32 s6, v64
	v_readfirstlane_b32 s7, v65
	v_readfirstlane_b32 s8, v66
	v_readfirstlane_b32 s9, v67
	s_nop 3
	s_add_u32 s10, s6, s7
	s_add_u32 s10, s10, s8
	s_add_u32 s10, s10, s9
	s_cmp_gt_u32 s27, 0
	s_cselect_b32 s14, s6, 0
	s_cmp_gt_u32 s27, 1
	s_cselect_b32 s15, s7, 0
	s_cmp_gt_u32 s27, 2
	s_cselect_b32 s16, s8, 0
	s_add_u32 s11, s14, s15
	s_add_u32 s11, s11, s16
	v_sub_u32_e32 v68, v50, v49
	v_sub_u32_e32 v69, v51, v59
	v_add_u32_e32 v68, s11, v68
	v_add_u32_e32 v69, s10, v69
	v_add_u32_e32 v70, v68, v49
	v_add_u32_e32 v71, v69, v59
	v_mov_b32_e32 v36, v0
	v_sub_u32_e32 v37, s2, v68
	v_mov_b32_e32 v38, v48
	v_mov_b32_e32 v39, v3
	v_or_b32_e32 v60, 0x100, v0
	v_sub_u32_e32 v61, s2, v69
	v_mov_b32_e32 v62, v58
	v_mov_b32_e32 v63, v5
	v_cmp_ge_u32_e64 s[14:15], s2, v68
	v_cmp_lt_u32_e64 s[16:17], s2, v70
	v_cmp_ge_u32_e64 s[6:7], s2, v69
	v_cmp_lt_u32_e64 s[8:9], s2, v71
	s_and_b64 s[14:15], s[14:15], s[16:17]
	s_and_b64 s[6:7], s[6:7], s[8:9]
	s_and_saveexec_b64 s[16:17], s[14:15]
	ds_write_b128 v34, v[36:39] offset:54144
	ds_write_b128 v34, v[42:45] offset:54160
	ds_write_b96 v34, v[46:48] offset:54176
	s_mov_b64 exec, s[16:17]
	s_and_saveexec_b64 s[16:17], s[6:7]
	ds_write_b128 v34, v[60:63] offset:54144
	ds_write_b128 v34, v[52:55] offset:54160
	ds_write_b96 v34, v[56:58] offset:54176
	s_mov_b64 exec, s[16:17]
	v_mov_b32_e32 v1, 0
	s_waitcnt lgkmcnt(0)
	s_barrier
	ds_read_b32 v2, v1 offset:54144
	s_waitcnt lgkmcnt(0)
	v_cmp_gt_i32_e32 vcc, 0, v2
	v_readfirstlane_b32 s2, v2
	s_cbranch_vccnz .LBB3_39
	v_mov_b32_e32 v5, 0xd39c
	s_load_dwordx2 s[22:23], s[0:1], 0x8
	s_load_dwordx2 s[18:19], s[0:1], 0x18
	v_mov_b32_e32 v2, 0xd384
	v_mov_b32_e32 v3, 0xd38c
	v_mov_b32_e32 v4, 0xd394
	ds_read2_b32 v[8:9], v5 offset1:1
	ds_read2_b32 v[6:7], v2 offset1:1
	ds_read2_b32 v[12:13], v3 offset1:1
	ds_read2_b32 v[10:11], v4 offset1:1
	ds_read_b32 v1, v1 offset:54180
	s_mov_b32 s28, 0
	s_add_u32 s1, s28, 16
	s_sub_u32 s3, 47, s1
	s_mul_i32 s3, s3, s1
	s_lshr_b32 s3, s3, 1
	s_cmp_ge_u32 s2, s3
	s_cselect_b32 s28, s1, s28
	s_add_u32 s1, s28, 8
	s_sub_u32 s3, 47, s1
	s_mul_i32 s3, s3, s1
	s_lshr_b32 s3, s3, 1
	s_cmp_ge_u32 s2, s3
	s_cselect_b32 s28, s1, s28
	s_add_u32 s1, s28, 4
	s_sub_u32 s3, 47, s1
	s_mul_i32 s3, s3, s1
	s_lshr_b32 s3, s3, 1
	s_cmp_ge_u32 s2, s3
	s_cselect_b32 s28, s1, s28
	s_add_u32 s1, s28, 2
	s_sub_u32 s3, 47, s1
	s_mul_i32 s3, s3, s1
	s_lshr_b32 s3, s3, 1
	s_cmp_ge_u32 s2, s3
	s_cselect_b32 s28, s1, s28
	s_add_u32 s1, s28, 1
	s_sub_u32 s3, 47, s1
	s_mul_i32 s3, s3, s1
	s_lshr_b32 s3, s3, 1
	s_cmp_ge_u32 s2, s3
	s_cselect_b32 s28, s1, s28
	s_sub_u32 s3, 47, s28
	s_mul_i32 s3, s3, s28
	s_lshr_b32 s3, s3, 1
	s_sub_u32 s0, s2, s3
	s_add_i32 s29, s28, s0
	s_add_i32 s29, s29, 1
	s_mul_hi_u32 s4, s2, 0x20680
	s_mul_i32 s5, s2, 0x20680
	v_lshrrev_b32_e32 v2, 6, v0
	s_movk_i32 s2, 0x180
	v_mov_b32_e32 v24, s29
	v_mov_b32_e32 v25, s28
	v_cmp_gt_u32_e32 vcc, s2, v0
	v_add_u32_e32 v4, -6, v2
	s_waitcnt lgkmcnt(0)
	v_lshlrev_b32_e32 v6, 7, v6
	v_cndmask_b32_e32 v3, v24, v25, vcc
	v_cndmask_b32_e32 v2, v4, v2, vcc
	v_mad_u64_u32 v[2:3], s[2:3], v3, 6, v[2:3]
	v_or_b32_e32 v4, 0x100, v0
	v_lshrrev_b32_e32 v4, 6, v4
	s_movk_i32 s2, 0x80
	v_cmp_gt_u32_e32 vcc, s2, v0
	v_add_u32_e32 v14, -6, v4
	s_lshl_b32 s0, s27, 5
	v_cndmask_b32_e32 v5, v24, v25, vcc
	v_cndmask_b32_e32 v4, v14, v4, vcc
	v_add_u32_e32 v36, s0, v6
	s_add_u32 s0, s20, 0x20000
	v_lshl_or_b32 v2, v2, 6, v92
	v_mad_u64_u32 v[4:5], s[2:3], v5, 6, v[4:5]
	s_addc_u32 s1, s21, 0
	v_ashrrev_i32_e32 v3, 31, v2
	v_lshl_or_b32 v4, v4, 6, v92
	v_lshl_add_u64 v[2:3], v[2:3], 4, s[0:1]
	v_ashrrev_i32_e32 v5, 31, v4
	v_lshl_add_u64 v[4:5], v[4:5], 4, s[0:1]
	global_load_dwordx4 v[16:19], v[2:3], off
	global_load_dwordx4 v[20:23], v[4:5], off
	v_or_b32_e32 v2, 0x200, v0
	v_lshrrev_b32_e32 v2, 6, v2
	v_mad_u64_u32 v[2:3], s[2:3], s29, 6, v[2:3]
	v_lshl_or_b32 v2, v2, 6, v92
	v_add_u32_e32 v14, 0xfffffe80, v2
	v_mov_b32_e32 v15, 0
	v_lshl_add_u64 v[28:29], v[14:15], 4, s[0:1]
	s_add_u32 s0, s20, s5
	v_min_u32_e32 v2, 47, v0
	s_addc_u32 s1, s21, s4
	v_cmp_gt_u32_e32 vcc, 24, v0
	v_subrev_u32_e32 v4, 24, v2
	s_add_u32 s24, s0, 0x800000
	v_cndmask_b32_e32 v3, v24, v25, vcc
	v_cndmask_b32_e32 v2, v4, v2, vcc
	s_addc_u32 s25, s1, 0
	v_mad_u64_u32 v[2:3], s[0:1], v3, 24, v[2:3]
	v_mov_b32_e32 v3, v15
	v_lshl_add_u64 v[2:3], v[2:3], 4, s[20:21]
	s_movk_i32 s0, 0x1000
	v_and_or_b32 v32, v0, 31, v36
	v_add_co_u32_e32 v30, vcc, s0, v2
	v_cmp_lt_i32_e64 s[0:1], v32, v7
	s_nop 0
	v_addc_co_u32_e32 v31, vcc, 0, v3, vcc
	v_cndmask_b32_e64 v14, v36, v32, s[0:1]
	v_cmp_lt_i32_e32 vcc, v36, v7
	global_load_dwordx4 v[24:27], v[28:29], off
	global_load_dwordx4 v[2:5], v[30:31], off
	v_cndmask_b32_e32 v14, v6, v14, vcc
	v_cmp_lt_i32_e64 s[2:3], v14, v12
	v_cmp_lt_i32_e64 s[4:5], v14, v13
	v_mov_b32_e32 v37, 0x1034
	v_cndmask_b32_e64 v28, v12, 0, s[2:3]
	v_cndmask_b32_e64 v28, v13, v28, s[4:5]
	v_cmp_lt_i32_e64 s[6:7], v14, v10
	v_cndmask_b32_e64 v29, v37, 0, s[2:3]
	v_mov_b32_e32 v38, 0x2068
	v_cndmask_b32_e64 v28, v10, v28, s[6:7]
	v_cmp_lt_i32_e64 s[8:9], v14, v11
	v_cndmask_b32_e64 v29, v38, v29, s[4:5]
	v_mov_b32_e32 v39, 0x309c
	v_cndmask_b32_e64 v28, v11, v28, s[8:9]
	v_cmp_lt_i32_e64 s[10:11], v14, v8
	v_cndmask_b32_e64 v29, v39, v29, s[6:7]
	v_mov_b32_e32 v40, 0x40d0
	v_cndmask_b32_e64 v28, v8, v28, s[10:11]
	v_cmp_lt_i32_e64 s[14:15], v14, v9
	v_cndmask_b32_e64 v29, v40, v29, s[8:9]
	v_mov_b32_e32 v41, 0x5104
	v_cndmask_b32_e64 v28, v9, v28, s[14:15]
	v_cmp_lt_i32_e64 s[16:17], v14, v1
	v_cndmask_b32_e64 v29, v41, v29, s[10:11]
	v_mov_b32_e32 v42, 0x6138
	v_cndmask_b32_e64 v28, v1, v28, s[16:17]
	v_cndmask_b32_e64 v29, v42, v29, s[14:15]
	v_mov_b32_e32 v43, 0x716c
	v_cndmask_b32_e64 v29, v43, v29, s[16:17]
	v_sub_u32_e32 v14, v14, v28
	v_add_u32_e32 v28, v14, v29
	v_lshrrev_b32_e32 v14, 3, v92
	v_or_b32_e32 v14, v36, v14
	v_cmp_lt_i32_e64 s[2:3], v14, v7
	v_ashrrev_i32_e32 v29, 31, v28
	v_lshl_add_u64 v[28:29], v[28:29], 2, s[24:25]
	v_cndmask_b32_e64 v30, v36, v14, s[2:3]
	v_cndmask_b32_e32 v30, v6, v30, vcc
	v_cmp_lt_i32_e64 s[2:3], v30, v12
	v_cmp_lt_i32_e64 s[4:5], v30, v13
	v_cmp_lt_i32_e64 s[6:7], v30, v10
	v_cndmask_b32_e64 v31, v12, 0, s[2:3]
	v_cndmask_b32_e64 v31, v13, v31, s[4:5]
	v_cndmask_b32_e64 v32, v37, 0, s[2:3]
	v_cndmask_b32_e64 v31, v10, v31, s[6:7]
	v_cmp_lt_i32_e64 s[8:9], v30, v11
	v_cndmask_b32_e64 v32, v38, v32, s[4:5]
	v_cmp_lt_i32_e64 s[10:11], v30, v8
	v_cndmask_b32_e64 v31, v11, v31, s[8:9]
	v_cndmask_b32_e64 v32, v39, v32, s[6:7]
	v_cndmask_b32_e64 v31, v8, v31, s[10:11]
	v_cmp_lt_i32_e64 s[14:15], v30, v9
	v_cndmask_b32_e64 v32, v40, v32, s[8:9]
	v_cmp_lt_i32_e64 s[16:17], v30, v1
	v_cndmask_b32_e64 v31, v9, v31, s[14:15]
	v_cndmask_b32_e64 v32, v41, v32, s[10:11]
	v_cndmask_b32_e64 v31, v1, v31, s[16:17]
	v_cndmask_b32_e64 v32, v42, v32, s[14:15]
	v_cndmask_b32_e64 v32, v43, v32, s[16:17]
	v_sub_u32_e32 v30, v30, v31
	v_add_u32_e32 v30, v30, v32
	v_or_b32_e32 v32, 8, v14
	v_cmp_lt_i32_e64 s[2:3], v32, v7
	v_ashrrev_i32_e32 v31, 31, v30
	v_lshl_add_u64 v[30:31], v[30:31], 2, s[24:25]
	v_cndmask_b32_e64 v32, v36, v32, s[2:3]
	v_cndmask_b32_e32 v32, v6, v32, vcc
	v_cmp_lt_i32_e64 s[2:3], v32, v12
	v_cmp_lt_i32_e64 s[4:5], v32, v13
	v_cmp_lt_i32_e64 s[6:7], v32, v10
	v_cndmask_b32_e64 v33, v12, 0, s[2:3]
	v_cndmask_b32_e64 v33, v13, v33, s[4:5]
	v_cndmask_b32_e64 v34, v37, 0, s[2:3]
	v_cndmask_b32_e64 v33, v10, v33, s[6:7]
	v_cmp_lt_i32_e64 s[8:9], v32, v11
	v_cndmask_b32_e64 v34, v38, v34, s[4:5]
	v_cmp_lt_i32_e64 s[10:11], v32, v8
	v_cndmask_b32_e64 v33, v11, v33, s[8:9]
	v_cndmask_b32_e64 v34, v39, v34, s[6:7]
	v_cndmask_b32_e64 v33, v8, v33, s[10:11]
	v_cmp_lt_i32_e64 s[14:15], v32, v9
	v_cndmask_b32_e64 v34, v40, v34, s[8:9]
	v_cmp_lt_i32_e64 s[16:17], v32, v1
	v_cndmask_b32_e64 v33, v9, v33, s[14:15]
	v_cndmask_b32_e64 v34, v41, v34, s[10:11]
	v_cndmask_b32_e64 v33, v1, v33, s[16:17]
	v_cndmask_b32_e64 v34, v42, v34, s[14:15]
	v_cndmask_b32_e64 v34, v43, v34, s[16:17]
	v_sub_u32_e32 v32, v32, v33
	v_add_u32_e32 v32, v32, v34
	v_or_b32_e32 v34, 16, v14
	v_cmp_lt_i32_e64 s[2:3], v34, v7
	v_or_b32_e32 v14, 24, v14
	v_ashrrev_i32_e32 v33, 31, v32
	v_cndmask_b32_e64 v34, v36, v34, s[2:3]
	v_cndmask_b32_e32 v34, v6, v34, vcc
	v_cmp_lt_i32_e64 s[2:3], v34, v12
	v_cmp_lt_i32_e64 s[4:5], v34, v13
	v_cmp_lt_i32_e64 s[6:7], v34, v10
	v_cndmask_b32_e64 v35, v12, 0, s[2:3]
	v_cndmask_b32_e64 v44, v37, 0, s[2:3]
	v_cmp_lt_i32_e64 s[2:3], v14, v7
	v_cndmask_b32_e64 v35, v13, v35, s[4:5]
	v_cndmask_b32_e64 v44, v38, v44, s[4:5]
	v_cndmask_b32_e64 v14, v36, v14, s[2:3]
	v_cndmask_b32_e32 v6, v6, v14, vcc
	v_cmp_lt_i32_e32 vcc, v6, v12
	v_cmp_lt_i32_e64 s[2:3], v6, v13
	v_cmp_lt_i32_e64 s[4:5], v6, v10
	v_cndmask_b32_e64 v12, v12, 0, vcc
	v_cndmask_b32_e64 v12, v13, v12, s[2:3]
	v_cndmask_b32_e64 v35, v10, v35, s[6:7]
	v_cmp_lt_i32_e64 s[8:9], v34, v11
	v_cndmask_b32_e64 v44, v39, v44, s[6:7]
	v_cndmask_b32_e64 v10, v10, v12, s[4:5]
	v_cmp_lt_i32_e64 s[6:7], v6, v11
	v_cndmask_b32_e64 v35, v11, v35, s[8:9]
	v_cmp_lt_i32_e64 s[10:11], v34, v8
	v_cndmask_b32_e64 v44, v40, v44, s[8:9]
	v_cndmask_b32_e64 v10, v11, v10, s[6:7]
	v_cmp_lt_i32_e64 s[8:9], v6, v8
	v_cndmask_b32_e64 v35, v8, v35, s[10:11]
	v_cmp_lt_i32_e64 s[14:15], v34, v9
	v_cndmask_b32_e64 v44, v41, v44, s[10:11]
	v_cndmask_b32_e64 v8, v8, v10, s[8:9]
	v_cmp_lt_i32_e64 s[10:11], v6, v9
	v_cndmask_b32_e64 v35, v9, v35, s[14:15]
	v_cmp_lt_i32_e64 s[16:17], v34, v1
	v_cndmask_b32_e64 v44, v42, v44, s[14:15]
	v_cndmask_b32_e64 v8, v9, v8, s[10:11]
	v_cmp_lt_i32_e64 s[14:15], v6, v1
	v_cndmask_b32_e64 v35, v1, v35, s[16:17]
	v_cndmask_b32_e64 v44, v43, v44, s[16:17]
	v_cndmask_b32_e64 v1, v1, v8, s[14:15]
	v_cndmask_b32_e64 v8, v37, 0, vcc
	v_cndmask_b32_e64 v8, v38, v8, s[2:3]
	v_cndmask_b32_e64 v8, v39, v8, s[4:5]
	v_cndmask_b32_e64 v8, v40, v8, s[6:7]
	v_cndmask_b32_e64 v8, v41, v8, s[8:9]
	v_cndmask_b32_e64 v8, v42, v8, s[10:11]
	v_sub_u32_e32 v34, v34, v35
	v_cndmask_b32_e64 v8, v43, v8, s[14:15]
	v_sub_u32_e32 v1, v6, v1
	v_add_u32_e32 v34, v34, v44
	v_add_u32_e32 v8, v1, v8
	v_ashrrev_i32_e32 v35, 31, v34
	v_ashrrev_i32_e32 v9, 31, v8
	v_lshl_add_u64 v[32:33], v[32:33], 2, s[24:25]
	v_lshl_add_u64 v[34:35], v[34:35], 2, s[24:25]
	v_lshl_add_u64 v[10:11], v[8:9], 2, s[24:25]
	global_load_dword v80, v[28:29], off
	global_load_dword v9, v[30:31], off
	global_load_dword v8, v[32:33], off
	global_load_dword v6, v[34:35], off
	global_load_dword v1, v[10:11], off
	v_cmp_ge_i32_e32 vcc, v36, v7
	v_lshlrev_b32_e32 v7, 4, v0
	s_waitcnt vmcnt(8)
	ds_write_b128 v7, v[16:19] offset:40960
	s_waitcnt vmcnt(7)
	ds_write_b128 v7, v[20:23] offset:45056
	s_waitcnt vmcnt(6)
	ds_write_b128 v7, v[24:27] offset:49152
	s_and_saveexec_b64 s[4:5], s[12:13]
	s_cbranch_execz .LBB3_31
	v_min_u32_e32 v10, 19, v0
	v_mov_b32_e32 v11, s29
	v_mov_b32_e32 v12, s28
	v_cmp_gt_u32_e64 s[2:3], 10, v0
	s_nop 1
	v_cndmask_b32_e64 v11, v11, v12, s[2:3]
	v_add_u32_e32 v12, -10, v10
	v_cndmask_b32_e64 v10, v12, v10, s[2:3]
	v_mad_u64_u32 v[10:11], s[2:3], v11, 10, v[10:11]
	v_mov_b32_e32 v11, v15
	v_lshl_add_u64 v[10:11], v[10:11], 2, s[22:23]
	global_load_dword v10, v[10:11], off
	v_mov_b32_e32 v11, 0xd300
	v_mov_b32_e32 v12, 0xd340
	v_cmp_lt_u32_e64 s[2:3], 9, v0
	s_nop 1
	v_cndmask_b32_e64 v11, v11, v12, s[2:3]
	v_add_u32_e32 v12, -10, v0
	v_min_u32_e32 v12, v0, v12
	v_lshl_add_u32 v11, v12, 2, v11
	s_waitcnt vmcnt(0)
	ds_write_b32 v11, v10
